# attention K/V band staging: steps 1 and 3 use v[242:249] so two load pairs are in flight per wait (two memory round trips instead of four) before the LDS writes
# baseline (speedup 1.0000x reference)
.LBB0_210:
	s_or_b64 exec, exec, s[2:3]
	v_readlane_b32 s2, v250, 15
	v_readlane_b32 s3, v250, 16
	s_or_b64 s[6:7], s[40:41], s[2:3]
	v_mov_b32_e32 v242, 0
	v_mov_b32_e32 v243, 0
	v_mov_b32_e32 v244, 0
	v_mov_b32_e32 v245, 0
	v_mov_b32_e32 v246, 0
	v_mov_b32_e32 v247, 0
	v_mov_b32_e32 v248, 0
	v_mov_b32_e32 v249, 0
	s_and_saveexec_b64 s[2:3], s[6:7]
	v_readlane_b32 s80, v251, 31
	v_readlane_b32 s82, v251, 33
	v_readlane_b32 s83, v251, 34
	s_mov_b32 s14, 0x40051592
	v_readlane_b32 s81, v251, 32
	v_readlane_b32 s84, v251, 35
	v_readlane_b32 s85, v251, 36
	v_readlane_b32 s86, v251, 37
	v_readlane_b32 s87, v251, 38
	v_readlane_b32 s88, v251, 39
	v_readlane_b32 s89, v251, 40
	v_readlane_b32 s90, v251, 41
	v_readlane_b32 s91, v251, 42
	v_readlane_b32 s92, v251, 43
	v_readlane_b32 s93, v251, 44
	v_readlane_b32 s94, v251, 45
	v_readlane_b32 s95, v251, 46
	s_cbranch_execz .LBB0_212
	v_add_u32_e32 v242, s5, v183
	v_ashrrev_i32_e32 v243, 31, v242
	v_lshlrev_b64 v[242:243], 9, v[242:243]
	v_readlane_b32 s6, v253, 18
	v_lshl_or_b32 v242, v14, 1, v242
	v_readlane_b32 s7, v253, 19
	s_nop 1
	v_lshl_add_u64 v[244:245], s[6:7], 0, v[242:243]
	v_readlane_b32 s6, v253, 16
	v_readlane_b32 s7, v253, 17
	s_nop 1
	v_lshl_add_u64 v[242:243], s[6:7], 0, v[242:243]
	global_load_dwordx4 v[246:249], v[242:243], off
	s_nop 0
	global_load_dwordx4 v[242:245], v[244:245], off
.LBB0_212:
	s_or_b64 exec, exec, s[2:3]
	v_readlane_b32 s2, v250, 17
	v_readlane_b32 s3, v250, 18
	s_waitcnt vmcnt(0)
	ds_write_b128 v189, v[10:13]
	ds_write_b128 v189, v[6:9] offset:36864
	ds_write_b128 v190, v[246:249]
	ds_write_b128 v190, v[242:245] offset:36864
	s_or_b64 s[6:7], s[40:41], s[2:3]
	v_mov_b32_e32 v5, 0
	v_mov_b32_e32 v6, 0
	v_mov_b32_e32 v7, 0
	v_mov_b32_e32 v8, 0
	v_mov_b32_e32 v9, 0
	v_mov_b32_e32 v10, 0
	v_mov_b32_e32 v11, 0
	s_and_saveexec_b64 s[2:3], s[6:7]
	s_cbranch_execz .LBB0_214
	v_add_u32_e32 v4, s5, v184
	v_ashrrev_i32_e32 v5, 31, v4
	v_lshlrev_b64 v[4:5], 9, v[4:5]
	v_readlane_b32 s6, v253, 18
	v_lshl_or_b32 v4, v14, 1, v4
	v_readlane_b32 s7, v253, 19
	s_nop 1
	v_lshl_add_u64 v[6:7], s[6:7], 0, v[4:5]
	v_readlane_b32 s6, v253, 16
	v_readlane_b32 s7, v253, 17
	s_nop 1
	v_lshl_add_u64 v[4:5], s[6:7], 0, v[4:5]
	global_load_dwordx4 v[8:11], v[4:5], off
	s_nop 0
	global_load_dwordx4 v[4:7], v[6:7], off
.LBB0_214:
	s_or_b64 exec, exec, s[2:3]
	v_readlane_b32 s2, v250, 19
	v_readlane_b32 s3, v250, 20
	s_or_b64 s[6:7], s[40:41], s[2:3]
	v_mov_b32_e32 v242, 0
	v_mov_b32_e32 v243, 0
	v_mov_b32_e32 v244, 0
	v_mov_b32_e32 v245, 0
	v_mov_b32_e32 v246, 0
	v_mov_b32_e32 v247, 0
	v_mov_b32_e32 v248, 0
	v_mov_b32_e32 v249, 0
	s_and_saveexec_b64 s[2:3], s[6:7]
	s_cbranch_execz .LBB0_216
	v_add_u32_e32 v242, s5, v185
	v_ashrrev_i32_e32 v243, 31, v242
	v_lshlrev_b64 v[242:243], 9, v[242:243]
	v_readlane_b32 s6, v253, 18
	v_lshl_or_b32 v242, v14, 1, v242
	v_readlane_b32 s7, v253, 19
	s_nop 1
	v_lshl_add_u64 v[244:245], s[6:7], 0, v[242:243]
	v_readlane_b32 s6, v253, 16
	v_readlane_b32 s7, v253, 17
	s_nop 1
	v_lshl_add_u64 v[242:243], s[6:7], 0, v[242:243]
	global_load_dwordx4 v[246:249], v[242:243], off
	s_nop 0
	global_load_dwordx4 v[242:245], v[244:245], off
.LBB0_216:
	s_or_b64 exec, exec, s[2:3]
	s_lshl_b32 s10, s4, 3
	s_waitcnt vmcnt(0)
	ds_write_b128 v191, v[8:11]
	ds_write_b128 v191, v[4:7] offset:36864
	ds_write_b128 v192, v[246:249]
	ds_write_b128 v192, v[242:245] offset:36864
	s_mov_b64 s[2:3], exec
	v_readlane_b32 s4, v250, 11
	v_readlane_b32 s5, v250, 12
	s_and_b64 s[4:5], s[2:3], s[4:5]
	s_mov_b64 exec, s[4:5]
	s_cbranch_execz .LBB0_223
	s_mov_b64 s[4:5], 0
	v_mov_b32_e32 v4, v186
	v_mov_b32_e32 v5, v1
	s_branch .LBB0_220
